# v7
# speedup vs baseline: 1.0824x; 1.0099x over previous
_Z9nerf_mainPKfS0_S0_PKiS2_PKcS0_Pf:
	s_load_dwordx8 s[8:15], s[0:1], 0x20
	s_load_dwordx8 s[24:31], s[0:1], 0x0
	v_readfirstlane_b32 s3, v0
	v_and_b32_e32 v120, 63, v0
	v_lshlrev_b32_e32 v121, 4, v120
	s_mov_b32 s39, 0x20000
	s_waitcnt lgkmcnt(0)
	s_load_dword s50, s[30:31], 0x0
	s_load_dword s51, s[8:9], 0x0
	s_load_dwordx8 s[52:59], s[28:29], 0x0
	s_load_dwordx4 s[60:63], s[28:29], 0x20
	s_lshr_b32 s64, s3, 7
	s_lshl_b32 s65, s2, 2
	s_add_i32 s64, s64, s65
	s_ashr_i32 s65, s64, 31
	s_lshl_b64 s[64:65], s[64:65], 2
	s_add_u32 s66, s24, s64
	s_addc_u32 s67, s25, s65
	s_add_u32 s64, s26, s64
	s_addc_u32 s65, s27, s65
	s_load_dword s68, s[66:67], 0x0
	s_load_dword s69, s[64:65], 0x0
	v_lshlrev_b32_e32 v188, 2, v0
	v_add_u32_e32 v189, 0x1000, v188
	global_load_dword v184, v188, s[12:13]
	global_load_dword v185, v188, s[12:13] offset:2048
	global_load_dword v186, v189, s[12:13]
	global_load_dword v187, v189, s[12:13] offset:2048
	s_and_b32 s37, s11, 0xffff
	s_lshl_b32 s11, s3, 4
	s_mov_b32 s38, 0xf0000
	s_and_b32 s42, s11, 0xfffffc00
	s_mov_b32 s4, s10
	s_mov_b32 s5, s37
	s_mov_b32 s6, s38
	s_mov_b32 s7, s39
	v_or_b32_e32 v125, s42, v121
	s_add_i32 m0, s42, 0x1a000
	s_movk_i32 s11, 0x2000
	buffer_load_dwordx4 v125, s[4:7], 0 offen lds
	s_add_i32 m0, s42, 0x1c000
	s_nop 0
	buffer_load_dwordx4 v125, s[4:7], s11 offen lds
	s_add_i32 m0, s42, 0x1e000
	s_movk_i32 s11, 0x4000
	buffer_load_dwordx4 v125, s[4:7], s11 offen lds
	s_add_i32 m0, s42, 0x20000
	s_movk_i32 s11, 0x6000
	buffer_load_dwordx4 v125, s[4:7], s11 offen lds
	s_add_i32 m0, s42, 0x22000
	s_mov_b32 s11, 0xe8000
	buffer_load_dwordx4 v125, s[4:7], s11 offen lds
	s_mov_b32 s36, s10
	s_waitcnt lgkmcnt(0)
	s_mov_b32 s0, s50
	s_lshl_b32 s1, s2, 2
	s_mov_b32 s2, s51
	s_lshr_b32 s31, s3, 7
	s_bfe_u32 s30, s3, 0x10006
	s_waitcnt lgkmcnt(0)
	v_cvt_f32_i32_e32 v1, s0
	s_add_i32 s12, s31, s1
	s_add_i32 s1, s0, 0xf423f
	s_cmp_lt_u32 s1, 0x1e847f
	v_mov_b32_e32 v2, s0
	s_cselect_b64 vcc, -1, 0
	v_cndmask_b32_e32 v123, v2, v1, vcc
	v_cvt_f32_i32_e32 v1, s2
	s_add_i32 s0, s2, 0xf423f
	s_cmp_lt_u32 s0, 0x1e847f
	v_mov_b32_e32 v2, s2
	s_cselect_b64 vcc, -1, 0
	v_cndmask_b32_e32 v1, v2, v1, vcc
	v_sub_f32_e32 v122, v1, v123
	s_mov_b32 s2, 0x427c0000
	v_div_scale_f32 v1, s[0:1], s2, s2, v122
	v_rcp_f32_e32 v2, v1
	s_ashr_i32 s13, s12, 31
	s_lshl_b64 s[0:1], s[12:13], 2
	s_add_u32 s4, s24, s0
	v_fma_f32 v5, -v1, v2, 1.0
	s_addc_u32 s5, s25, s1
	v_fmac_f32_e32 v2, v5, v2
	v_div_scale_f32 v5, vcc, v122, s2, v122
	s_add_u32 s0, s26, s0
	v_mul_f32_e32 v6, v5, v2
	s_mov_b64 s[16:17], s[52:53]
	s_mov_b64 s[18:19], s[54:55]
	s_mov_b64 s[20:21], s[56:57]
	s_mov_b64 s[22:23], s[58:59]
	s_addc_u32 s1, s27, s1
	v_fma_f32 v7, -v1, v6, v5
	s_mov_b32 s4, s68
	v_fmac_f32_e32 v6, v7, v2
	s_mov_b32 s0, s69
	v_fma_f32 v1, -v1, v6, v5
	v_div_fmas_f32 v1, v1, v2, v6
	v_div_fixup_f32 v124, v1, s2, v122
	s_waitcnt lgkmcnt(0)
	v_mov_b32_e32 v1, s16
	s_mov_b64 s[24:25], s[60:61]
	s_mov_b64 s[26:27], s[62:63]
	v_mul_f32_e32 v1, s4, v1
	v_mov_b32_e32 v2, s0
	v_fma_f32 v1, s17, -v2, v1
	v_add_f32_e32 v127, s19, v1
	v_mov_b32_e32 v1, s20
	v_mul_f32_e32 v1, s4, v1
	v_fma_f32 v1, s21, -v2, v1
	v_add_f32_e32 v128, s23, v1
	s_waitcnt lgkmcnt(0)
	v_mov_b32_e32 v1, s24
	v_mul_f32_e32 v1, s4, v1
	v_and_b32_e32 v3, 15, v0
	v_fma_f32 v1, s25, -v2, v1
	v_and_b32_e32 v131, 48, v0
	v_lshl_or_b32 v0, s30, 6, v120
	v_add_f32_e32 v129, s27, v1
	v_add_u32_e32 v1, 1, v0
	v_cvt_f32_ubyte0_e32 v1, v1
	s_mov_b32 s4, 0x43010000
	s_and_b32 s19, s3, 0xffffff80
	v_div_scale_f32 v2, s[2:3], s4, s4, v1
	v_lshl_or_b32 v130, s30, 5, v3
	v_rcp_f32_e32 v3, v2
	v_lshrrev_b32_e32 v4, 4, v120
	v_cmp_eq_u32_e64 s[8:9], 2, v4
	v_cmp_eq_u32_e64 s[10:11], 1, v4
	v_fma_f32 v5, -v2, v3, 1.0
	v_fmac_f32_e32 v3, v5, v3
	v_div_scale_f32 v5, vcc, v1, s4, v1
	v_mul_f32_e32 v6, v5, v3
	v_fma_f32 v7, -v2, v6, v5
	v_fmac_f32_e32 v6, v7, v3
	v_fma_f32 v2, -v2, v6, v5
	v_div_fmas_f32 v2, v2, v3, v6
	v_div_fixup_f32 v134, v2, s4, v1
	v_add_u32_e32 v2, -1, v4
	v_cmp_gt_u32_e32 vcc, 2, v2
	v_mov_b32_e32 v2, 0x401550d3
	v_mov_b32_e32 v3, 0x436d0620
	v_cndmask_b32_e64 v5, v2, v3, s[8:9]
	v_mov_b32_e32 v6, 0x412e2e5e
	v_cmp_eq_u32_e64 s[0:1], 3, v4
	v_cndmask_b32_e64 v4, v5, v6, s[10:11]
	v_cmp_gt_u32_e64 s[2:3], 16, v120
	v_bfrev_b32_e32 v5, 34
	v_mov_b32_e32 v8, 0x41bc2043
	v_cndmask_b32_e64 v140, v4, 0.5, s[2:3]
	v_mov_b32_e32 v4, 0x40a14518
	v_cndmask_b32_e64 v7, v4, v5, s[8:9]
	v_cndmask_b32_e64 v7, v7, v8, s[10:11]
	v_mov_b32_e32 v9, 0x3f8a3f66
	v_cndmask_b32_e64 v141, v7, v9, s[2:3]
	v_cndmask_b32_e64 v7, v6, 0.5, s[8:9]
	v_cndmask_b32_e64 v6, v3, v6, s[8:9]
	v_mov_b32_e32 v10, 0x424b2ff5
	v_cndmask_b32_e64 v6, v6, 0.5, s[10:11]
	v_cndmask_b32_e64 v144, v6, v10, s[2:3]
	v_cndmask_b32_e64 v6, v5, v8, s[8:9]
	v_or_b32_e32 v0, s19, v0
	v_mov_b32_e32 v11, 0x42db7457
	v_cndmask_b32_e64 v6, v6, v9, s[10:11]
	v_lshlrev_b32_e32 v0, 2, v0
	v_cndmask_b32_e64 v7, v7, v10, s[10:11]
	v_cndmask_b32_e64 v145, v6, v11, s[2:3]
	v_cndmask_b32_e64 v6, 0, v10, s[8:9]
	v_add_u32_e32 v135, 0x15000, v0
	v_add_u32_e32 v136, 0x15800, v0
	v_cvt_f32_ubyte0_e32 v0, v130
	v_or_b32_e32 v138, 16, v130
	v_cndmask_b32_e64 v142, v7, v2, s[2:3]
	v_cndmask_b32_e64 v2, v6, v2, s[10:11]
	s_lshl_b32 s13, s31, 10
	s_lshl_b32 s44, s31, 8
	v_fma_f32 v137, v0, v124, v123
	v_cvt_f32_ubyte0_e32 v0, v138
	v_cndmask_b32_e64 v7, v8, v9, s[8:9]
	v_cndmask_b32_e64 v146, v2, v3, s[2:3]
	v_cndmask_b32_e64 v2, 0, v11, s[8:9]
	s_lshl_b32 s27, s19, 2
	s_add_i32 s13, s13, 0x12000
	s_add_i32 s44, s44, 0x16000
	v_fma_f32 v139, v0, v124, v123
	v_lshlrev_b32_e32 v0, 4, v130
	v_lshlrev_b32_e32 v1, 4, v138
	v_cndmask_b32_e64 v7, v7, v11, s[10:11]
	v_cndmask_b32_e64 v2, v2, v4, s[10:11]
	v_or_b32_e32 v126, 0x2000, v121
	s_add_i32 s23, s27, 0x15000
	s_add_i32 s28, s42, 0xa000
	s_add_i32 s29, s42, 0xc000
	s_add_i32 s33, s42, 0xe000
	s_add_i32 s34, s42, 0x10000
	s_add_i32 s35, s42, 0x2000
	s_add_i32 s40, s42, 0x8000
	s_add_i32 s41, s42, 0x6000
	s_addk_i32 s42, 0x4000
	s_sub_i32 s43, s19, 64
	v_lshl_or_b32 v132, v120, 4, s13
	v_lshl_or_b32 v133, v120, 2, s44
	s_mov_b32 s20, 1
	s_or_b64 s[4:5], s[2:3], vcc
	s_or_b64 s[6:7], s[2:3], s[10:11]
	v_cndmask_b32_e64 v143, v7, v4, s[2:3]
	s_mov_b32 s45, 0
	v_cndmask_b32_e64 v147, v2, v5, s[2:3]
	v_or_b32_e32 v148, 0x1a000, v121
	v_or_b32_e32 v149, 0x1a400, v121
	v_or_b32_e32 v150, 0x1a800, v121
	v_or_b32_e32 v151, 0x1ac00, v121
	v_or_b32_e32 v152, 0x1b000, v121
	v_or_b32_e32 v153, 0x1b400, v121
	v_or_b32_e32 v154, 0x1b800, v121
	v_or_b32_e32 v155, 0x1bc00, v121
	v_or_b32_e32 v156, 0x1c000, v121
	v_or_b32_e32 v157, 0x1c400, v121
	v_or_b32_e32 v158, 0x1c800, v121
	v_or_b32_e32 v159, 0x1cc00, v121
	v_or_b32_e32 v160, 0x1d000, v121
	v_or_b32_e32 v161, 0x1d400, v121
	v_or_b32_e32 v162, 0x1d800, v121
	v_or_b32_e32 v163, 0x1dc00, v121
	v_or_b32_e32 v164, 0x1e000, v121
	v_or_b32_e32 v165, 0x1e400, v121
	v_or_b32_e32 v166, 0x1e800, v121
	v_or_b32_e32 v167, 0x1ec00, v121
	v_or_b32_e32 v168, 0x1f000, v121
	v_or_b32_e32 v169, 0x1f400, v121
	v_or_b32_e32 v170, 0x1f800, v121
	v_or_b32_e32 v171, 0x1fc00, v121
	v_or_b32_e32 v172, 0x20000, v121
	v_or_b32_e32 v173, 0x20400, v121
	v_or_b32_e32 v174, 0x20800, v121
	v_or_b32_e32 v175, 0x20c00, v121
	v_or_b32_e32 v176, 0x21000, v121
	v_or_b32_e32 v177, 0x21400, v121
	v_or_b32_e32 v178, 0x21800, v121
	v_or_b32_e32 v179, 0x21c00, v121
	v_add_u32_e32 v180, s13, v0
	v_add_u32_e32 v181, s13, v1
	v_mov_b32_e32 v182, 0x13000
	s_waitcnt vmcnt(0)
	ds_write_b32 v188, v184
	ds_write_b32 v188, v185 offset:2048
	ds_write_b32 v188, v186 offset:4096
	ds_write_b32 v188, v187 offset:6144
	s_branch .LBB1_5

.LBB1_9:
	s_waitcnt lgkmcnt(0)
	v_fma_f32 v2, s18, v1, v127
	v_fma_f32 v3, s22, v1, v128
	v_cndmask_b32_e64 v4, v3, v2, s[4:5]
	v_cndmask_b32_e64 v2, v3, v2, s[6:7]
	v_mul_f32_e32 v8, v2, v142
	v_mul_f32_e32 v2, v2, v143
	v_mul_f32_e32 v5, v4, v140
	v_mul_f32_e32 v4, v4, v141
	v_fract_f32_e32 v2, v2
	v_fract_f32_e32 v4, v4
	v_sin_f32_e32 v10, v2
	v_cos_f32_e32 v2, v2
	v_sin_f32_e32 v7, v4
	v_cos_f32_e32 v4, v4
	v_fma_f32 v1, s26, v1, v129
	v_fract_f32_e32 v5, v5
	v_sin_f32_e32 v6, v5
	v_cos_f32_e32 v5, v5
	v_cndmask_b32_e64 v1, v1, v3, s[2:3]
	v_cvt_pk_bf16_f32 v211, v10, v2
	v_mul_f32_e32 v2, v1, v144
	v_cvt_pk_bf16_f32 v209, v7, v4
	v_fract_f32_e32 v2, v2
	v_mul_f32_e32 v4, v1, v145
	v_sin_f32_e32 v3, v2
	v_cos_f32_e32 v2, v2
	v_fract_f32_e32 v4, v4
	v_cvt_pk_bf16_f32 v208, v6, v5
	v_sin_f32_e32 v5, v4
	v_cos_f32_e32 v4, v4
	v_mul_f32_e32 v6, v1, v146
	v_fract_f32_e32 v6, v6
	v_mul_f32_e32 v1, v1, v147
	v_cos_f32_e32 v7, v6
	v_cvt_pk_bf16_f32 v216, v3, v2
	v_sin_f32_e32 v2, v6
	v_fract_f32_e32 v1, v1
	v_cvt_pk_bf16_f32 v217, v5, v4
	v_cos_f32_e32 v4, v1
	v_sin_f32_e32 v1, v1
	v_cndmask_b32_e64 v3, v7, 0, s[0:1]
	v_cndmask_b32_e64 v2, v2, 1.0, s[0:1]
	v_fract_f32_e32 v8, v8
	v_cvt_pk_bf16_f32 v218, v2, v3
	v_cndmask_b32_e64 v2, v4, 0, s[0:1]
	v_cndmask_b32_e64 v1, v1, 0, s[0:1]
	v_sin_f32_e32 v9, v8
	v_cos_f32_e32 v8, v8
	v_cvt_pk_bf16_f32 v219, v1, v2
	v_fma_f32 v1, s18, v0, v127
	v_fma_f32 v2, s22, v0, v128
	v_cndmask_b32_e64 v3, v2, v1, s[4:5]
	v_cndmask_b32_e64 v1, v2, v1, s[6:7]
	v_mul_f32_e32 v7, v1, v142
	v_mul_f32_e32 v1, v1, v143
	v_mul_f32_e32 v4, v3, v140
	v_mul_f32_e32 v3, v3, v141
	v_fract_f32_e32 v1, v1
	v_cvt_pk_bf16_f32 v210, v9, v8
	v_fract_f32_e32 v3, v3
	v_sin_f32_e32 v9, v1
	v_cos_f32_e32 v1, v1
	v_sin_f32_e32 v6, v3
	v_cos_f32_e32 v3, v3
	v_fma_f32 v0, s26, v0, v129
	v_fract_f32_e32 v4, v4
	v_sin_f32_e32 v5, v4
	v_cos_f32_e32 v4, v4
	v_cndmask_b32_e64 v0, v0, v2, s[2:3]
	v_cvt_pk_bf16_f32 v215, v9, v1
	v_mul_f32_e32 v1, v0, v144
	v_cvt_pk_bf16_f32 v213, v6, v3
	v_fract_f32_e32 v1, v1
	v_mul_f32_e32 v3, v0, v145
	v_sin_f32_e32 v2, v1
	v_cos_f32_e32 v1, v1
	v_fract_f32_e32 v3, v3
	v_cvt_pk_bf16_f32 v212, v5, v4
	v_sin_f32_e32 v4, v3
	v_cos_f32_e32 v3, v3
	v_mul_f32_e32 v5, v0, v146
	v_fract_f32_e32 v5, v5
	v_mul_f32_e32 v0, v0, v147
	v_fract_f32_e32 v7, v7
	v_cos_f32_e32 v6, v5
	v_cvt_pk_bf16_f32 v220, v2, v1
	v_sin_f32_e32 v1, v5
	v_fract_f32_e32 v0, v0
	v_sin_f32_e32 v8, v7
	v_cos_f32_e32 v7, v7
	v_cvt_pk_bf16_f32 v221, v4, v3
	v_cos_f32_e32 v3, v0
	v_cndmask_b32_e64 v2, v6, 0, s[0:1]
	v_cndmask_b32_e64 v1, v1, 1.0, s[0:1]
	v_cvt_pk_bf16_f32 v214, v8, v7
	v_cvt_pk_bf16_f32 v222, v1, v2
	v_sin_f32_e32 v16, v0
	v_cndmask_b32_e64 v17, v3, 0, s[0:1]
	v_cndmask_b32_e64 v16, v16, 0, s[0:1]
	v_cvt_pk_bf16_f32 v223, v16, v17
	v_mov_b32_e32 v183, v131
	s_mov_b32 s50, 0x10000
	s_mov_b32 s52, 0
	v_add_u32_e32 v149, 0x22000, v121
	s_waitcnt vmcnt(0) lgkmcnt(0)
	s_barrier
	ds_read_b128 v[224:227], v148 offset:0
	ds_read_b128 v[228:231], v148 offset:1024
	ds_read_b128 v[232:235], v148 offset:2048
	ds_read_b128 v[236:239], v148 offset:3072
	ds_read_b128 v[240:243], v148 offset:4096
	ds_read_b128 v[244:247], v148 offset:5120
	ds_read_b128 v[248:251], v148 offset:6144
	ds_read_b128 v[252:255], v148 offset:7168
	s_waitcnt lgkmcnt(7)
	v_mfma_f32_16x16x32_bf16 v[64:67], v[224:227], v[208:211], 0
	v_mfma_f32_16x16x32_bf16 v[56:59], v[224:227], v[212:215], 0
	ds_read_b128 v[224:227], v148 offset:8192
	s_waitcnt lgkmcnt(7)
	v_mfma_f32_16x16x32_bf16 v[68:71], v[228:231], v[208:211], 0
	v_mfma_f32_16x16x32_bf16 v[60:63], v[228:231], v[212:215], 0
	ds_read_b128 v[228:231], v148 offset:9216
	s_waitcnt lgkmcnt(7)
	v_mfma_f32_16x16x32_bf16 v[64:67], v[232:235], v[216:219], v[64:67]
	v_mfma_f32_16x16x32_bf16 v[56:59], v[232:235], v[220:223], v[56:59]
	ds_read_b128 v[232:235], v148 offset:10240
	s_waitcnt lgkmcnt(7)
	v_mfma_f32_16x16x32_bf16 v[68:71], v[236:239], v[216:219], v[68:71]
	v_mfma_f32_16x16x32_bf16 v[60:63], v[236:239], v[220:223], v[60:63]
	ds_read_b128 v[236:239], v148 offset:11264
	s_waitcnt lgkmcnt(7)
	v_mfma_f32_16x16x32_bf16 v[80:83], v[240:243], v[208:211], 0
	v_cvt_pk_bf16_f32 v0, v64, v65
	v_cvt_pk_bf16_f32 v1, v66, v67
	v_mfma_f32_16x16x32_bf16 v[84:87], v[240:243], v[212:215], 0
	v_cvt_pk_bf16_f32 v4, v56, v57
	v_cvt_pk_bf16_f32 v5, v58, v59
	ds_read_b128 v[240:243], v148 offset:12288
	s_waitcnt lgkmcnt(7)
	v_mfma_f32_16x16x32_bf16 v[76:79], v[244:247], v[208:211], 0
	v_cvt_pk_bf16_f32 v2, v68, v69
	v_cvt_pk_bf16_f32 v3, v70, v71
	s_mov_b32 m0, s28
	s_mov_b32 s51, 0x8000
	v_mfma_f32_16x16x32_bf16 v[72:75], v[244:247], v[212:215], 0
	v_cvt_pk_bf16_f32 v6, v60, v61
	v_cvt_pk_bf16_f32 v7, v62, v63
	buffer_load_dwordx4 v125, s[36:39], s51 offen lds
	ds_read_b128 v[244:247], v148 offset:13312
	s_waitcnt lgkmcnt(7)
	v_mfma_f32_16x16x32_bf16 v[80:83], v[248:251], v[216:219], v[80:83]
	v_pk_max_i16 v0, v0, 0
	v_pk_max_i16 v1, v1, 0
	v_mfma_f32_16x16x32_bf16 v[84:87], v[248:251], v[220:223], v[84:87]
	v_pk_max_i16 v2, v2, 0
	v_pk_max_i16 v3, v3, 0
	ds_read_b128 v[248:251], v148 offset:14336
	s_waitcnt lgkmcnt(7)
	v_mfma_f32_16x16x32_bf16 v[76:79], v[252:255], v[216:219], v[76:79]
	v_pk_max_i16 v4, v4, 0
	v_pk_max_i16 v5, v5, 0
	v_mfma_f32_16x16x32_bf16 v[72:75], v[252:255], v[220:223], v[72:75]
	v_pk_max_i16 v6, v6, 0
	v_pk_max_i16 v7, v7, 0
	ds_read_b128 v[252:255], v148 offset:15360
	s_waitcnt lgkmcnt(7)
	v_mfma_f32_16x16x32_bf16 v[64:67], v[224:227], v[208:211], 0
	v_cvt_pk_bf16_f32 v12, v80, v81
	v_cvt_pk_bf16_f32 v13, v82, v83
	v_mfma_f32_16x16x32_bf16 v[56:59], v[224:227], v[212:215], 0
	v_cvt_pk_bf16_f32 v8, v84, v85
	v_cvt_pk_bf16_f32 v9, v86, v87
	ds_read_b128 v[224:227], v148 offset:16384
	s_waitcnt lgkmcnt(7)
	v_mfma_f32_16x16x32_bf16 v[68:71], v[228:231], v[208:211], 0
	v_cvt_pk_bf16_f32 v14, v76, v77
	v_cvt_pk_bf16_f32 v15, v78, v79
	s_mov_b32 m0, s29
	s_mov_b32 s51, 0xa000
	v_mfma_f32_16x16x32_bf16 v[60:63], v[228:231], v[212:215], 0
	v_cvt_pk_bf16_f32 v10, v72, v73
	v_cvt_pk_bf16_f32 v11, v74, v75
	buffer_load_dwordx4 v125, s[36:39], s51 offen lds
	ds_read_b128 v[228:231], v148 offset:17408
	s_waitcnt lgkmcnt(7)
	v_mfma_f32_16x16x32_bf16 v[64:67], v[232:235], v[216:219], v[64:67]
	v_pk_max_i16 v12, v12, 0
	v_pk_max_i16 v13, v13, 0
	v_mfma_f32_16x16x32_bf16 v[56:59], v[232:235], v[220:223], v[56:59]
	v_pk_max_i16 v14, v14, 0
	v_pk_max_i16 v15, v15, 0
	ds_read_b128 v[232:235], v148 offset:18432
	s_waitcnt lgkmcnt(7)
	v_mfma_f32_16x16x32_bf16 v[68:71], v[236:239], v[216:219], v[68:71]
	v_pk_max_i16 v8, v8, 0
	v_pk_max_i16 v9, v9, 0
	v_mfma_f32_16x16x32_bf16 v[60:63], v[236:239], v[220:223], v[60:63]
	v_pk_max_i16 v10, v10, 0
	v_pk_max_i16 v11, v11, 0
	ds_read_b128 v[236:239], v148 offset:19456
	s_waitcnt lgkmcnt(7)
	v_mfma_f32_16x16x32_bf16 v[80:83], v[240:243], v[208:211], 0
	v_cvt_pk_bf16_f32 v16, v64, v65
	v_cvt_pk_bf16_f32 v17, v66, v67
	v_mfma_f32_16x16x32_bf16 v[84:87], v[240:243], v[212:215], 0
	v_cvt_pk_bf16_f32 v20, v56, v57
	v_cvt_pk_bf16_f32 v21, v58, v59
	ds_read_b128 v[240:243], v148 offset:20480
	s_waitcnt lgkmcnt(7)
	v_mfma_f32_16x16x32_bf16 v[76:79], v[244:247], v[208:211], 0
	v_cvt_pk_bf16_f32 v18, v68, v69
	v_cvt_pk_bf16_f32 v19, v70, v71
	s_mov_b32 m0, s33
	s_mov_b32 s51, 0xc000
	v_mfma_f32_16x16x32_bf16 v[72:75], v[244:247], v[212:215], 0
	v_cvt_pk_bf16_f32 v22, v60, v61
	v_cvt_pk_bf16_f32 v23, v62, v63
	buffer_load_dwordx4 v125, s[36:39], s51 offen lds
	ds_read_b128 v[244:247], v148 offset:21504
	s_waitcnt lgkmcnt(7)
	v_mfma_f32_16x16x32_bf16 v[80:83], v[248:251], v[216:219], v[80:83]
	v_pk_max_i16 v16, v16, 0
	v_pk_max_i16 v17, v17, 0
	v_mfma_f32_16x16x32_bf16 v[84:87], v[248:251], v[220:223], v[84:87]
	v_pk_max_i16 v18, v18, 0
	v_pk_max_i16 v19, v19, 0
	ds_read_b128 v[248:251], v148 offset:22528
	s_waitcnt lgkmcnt(7)
	v_mfma_f32_16x16x32_bf16 v[76:79], v[252:255], v[216:219], v[76:79]
	v_pk_max_i16 v20, v20, 0
	v_pk_max_i16 v21, v21, 0
	v_mfma_f32_16x16x32_bf16 v[72:75], v[252:255], v[220:223], v[72:75]
	v_pk_max_i16 v22, v22, 0
	v_pk_max_i16 v23, v23, 0
	ds_read_b128 v[252:255], v148 offset:23552
	s_waitcnt lgkmcnt(7)
	v_mfma_f32_16x16x32_bf16 v[64:67], v[224:227], v[208:211], 0
	v_cvt_pk_bf16_f32 v24, v80, v81
	v_cvt_pk_bf16_f32 v25, v82, v83
	v_mfma_f32_16x16x32_bf16 v[56:59], v[224:227], v[212:215], 0
	v_cvt_pk_bf16_f32 v28, v84, v85
	v_cvt_pk_bf16_f32 v29, v86, v87
	ds_read_b128 v[224:227], v148 offset:24576
	s_waitcnt lgkmcnt(7)
	v_mfma_f32_16x16x32_bf16 v[68:71], v[228:231], v[208:211], 0
	v_cvt_pk_bf16_f32 v26, v76, v77
	v_cvt_pk_bf16_f32 v27, v78, v79
	s_mov_b32 m0, s34
	s_mov_b32 s51, 0xe000
	v_mfma_f32_16x16x32_bf16 v[60:63], v[228:231], v[212:215], 0
	v_cvt_pk_bf16_f32 v30, v72, v73
	v_cvt_pk_bf16_f32 v31, v74, v75
	buffer_load_dwordx4 v125, s[36:39], s51 offen lds
	ds_read_b128 v[228:231], v148 offset:25600
	s_waitcnt lgkmcnt(7)
	v_mfma_f32_16x16x32_bf16 v[64:67], v[232:235], v[216:219], v[64:67]
	v_pk_max_i16 v24, v24, 0
	v_pk_max_i16 v25, v25, 0
	v_mfma_f32_16x16x32_bf16 v[56:59], v[232:235], v[220:223], v[56:59]
	v_pk_max_i16 v26, v26, 0
	v_pk_max_i16 v27, v27, 0
	ds_read_b128 v[232:235], v148 offset:26624
	s_waitcnt lgkmcnt(7)
	v_mfma_f32_16x16x32_bf16 v[68:71], v[236:239], v[216:219], v[68:71]
	v_pk_max_i16 v28, v28, 0
	v_pk_max_i16 v29, v29, 0
	v_mfma_f32_16x16x32_bf16 v[60:63], v[236:239], v[220:223], v[60:63]
	v_pk_max_i16 v30, v30, 0
	v_pk_max_i16 v31, v31, 0
	ds_read_b128 v[236:239], v148 offset:27648
	s_waitcnt lgkmcnt(7)
	v_mfma_f32_16x16x32_bf16 v[80:83], v[240:243], v[208:211], 0
	v_cvt_pk_bf16_f32 v32, v64, v65
	v_cvt_pk_bf16_f32 v33, v66, v67
	v_mfma_f32_16x16x32_bf16 v[84:87], v[240:243], v[212:215], 0
	v_cvt_pk_bf16_f32 v36, v56, v57
	v_cvt_pk_bf16_f32 v37, v58, v59
	ds_read_b128 v[240:243], v148 offset:28672
	s_waitcnt lgkmcnt(7)
	v_mfma_f32_16x16x32_bf16 v[76:79], v[244:247], v[208:211], 0
	v_cvt_pk_bf16_f32 v34, v68, v69
	v_cvt_pk_bf16_f32 v35, v70, v71
	v_mfma_f32_16x16x32_bf16 v[72:75], v[244:247], v[212:215], 0
	v_cvt_pk_bf16_f32 v38, v60, v61
	v_cvt_pk_bf16_f32 v39, v62, v63
	ds_read_b128 v[244:247], v148 offset:29696
	s_waitcnt lgkmcnt(7)
	v_mfma_f32_16x16x32_bf16 v[80:83], v[248:251], v[216:219], v[80:83]
	v_pk_max_i16 v32, v32, 0
	v_pk_max_i16 v33, v33, 0
	v_mfma_f32_16x16x32_bf16 v[84:87], v[248:251], v[220:223], v[84:87]
	v_pk_max_i16 v34, v34, 0
	v_pk_max_i16 v35, v35, 0
	ds_read_b128 v[248:251], v148 offset:30720
	s_waitcnt lgkmcnt(7)
	v_mfma_f32_16x16x32_bf16 v[76:79], v[252:255], v[216:219], v[76:79]
	v_pk_max_i16 v36, v36, 0
	v_pk_max_i16 v37, v37, 0
	v_mfma_f32_16x16x32_bf16 v[72:75], v[252:255], v[220:223], v[72:75]
	v_pk_max_i16 v38, v38, 0
	v_pk_max_i16 v39, v39, 0
	ds_read_b128 v[252:255], v148 offset:31744
	s_waitcnt lgkmcnt(7)
	v_mfma_f32_16x16x32_bf16 v[64:67], v[224:227], v[208:211], 0
	v_cvt_pk_bf16_f32 v40, v80, v81
	v_cvt_pk_bf16_f32 v41, v82, v83
	v_mfma_f32_16x16x32_bf16 v[56:59], v[224:227], v[212:215], 0
	v_cvt_pk_bf16_f32 v44, v84, v85
	v_cvt_pk_bf16_f32 v45, v86, v87
	s_waitcnt lgkmcnt(6)
	v_mfma_f32_16x16x32_bf16 v[68:71], v[228:231], v[208:211], 0
	v_cvt_pk_bf16_f32 v42, v76, v77
	v_cvt_pk_bf16_f32 v43, v78, v79
	v_mfma_f32_16x16x32_bf16 v[60:63], v[228:231], v[212:215], 0
	v_cvt_pk_bf16_f32 v46, v72, v73
	v_cvt_pk_bf16_f32 v47, v74, v75
	s_waitcnt lgkmcnt(5)
	v_mfma_f32_16x16x32_bf16 v[64:67], v[232:235], v[216:219], v[64:67]
	v_pk_max_i16 v40, v40, 0
	v_pk_max_i16 v41, v41, 0
	v_mfma_f32_16x16x32_bf16 v[56:59], v[232:235], v[220:223], v[56:59]
	v_pk_max_i16 v42, v42, 0
	v_pk_max_i16 v43, v43, 0
	s_waitcnt lgkmcnt(4)
	v_mfma_f32_16x16x32_bf16 v[68:71], v[236:239], v[216:219], v[68:71]
	v_pk_max_i16 v44, v44, 0
	v_pk_max_i16 v45, v45, 0
	v_mfma_f32_16x16x32_bf16 v[60:63], v[236:239], v[220:223], v[60:63]
	v_pk_max_i16 v46, v46, 0
	v_pk_max_i16 v47, v47, 0
	s_cmp_lt_u32 s31, 2
	s_cbranch_scc0 .Lnerf_hid_b_first
	s_waitcnt vmcnt(0) lgkmcnt(0)
	s_barrier
	ds_read_b128 v[224:227], v121 offset:40960
	ds_read_b128 v[228:231], v121 offset:41984
	ds_read_b128 v[152:155], v183 offset:0
	ds_read_b128 v[156:159], v183 offset:64
	v_mfma_f32_16x16x32_bf16 v[80:83], v[240:243], v[208:211], 0
	ds_read_b128 v[232:235], v121 offset:43008
	v_cvt_pk_bf16_f32 v48, v64, v65
	v_cvt_pk_bf16_f32 v49, v66, v67
	v_mfma_f32_16x16x32_bf16 v[84:87], v[240:243], v[212:215], 0
	ds_read_b128 v[236:239], v121 offset:44032
	v_cvt_pk_bf16_f32 v52, v56, v57
	v_cvt_pk_bf16_f32 v53, v58, v59
	ds_read_b128 v[240:243], v121 offset:45056
	v_mfma_f32_16x16x32_bf16 v[76:79], v[244:247], v[208:211], 0
	v_cvt_pk_bf16_f32 v50, v68, v69
	v_cvt_pk_bf16_f32 v51, v70, v71
	v_mfma_f32_16x16x32_bf16 v[72:75], v[244:247], v[212:215], 0
	v_cvt_pk_bf16_f32 v54, v60, v61
	v_cvt_pk_bf16_f32 v55, v62, v63
	ds_read_b128 v[244:247], v121 offset:46080
	v_mfma_f32_16x16x32_bf16 v[80:83], v[248:251], v[216:219], v[80:83]
	v_pk_max_i16 v48, v48, 0
	v_pk_max_i16 v49, v49, 0
	v_mfma_f32_16x16x32_bf16 v[84:87], v[248:251], v[220:223], v[84:87]
	v_pk_max_i16 v50, v50, 0
	v_pk_max_i16 v51, v51, 0
	ds_read_b128 v[248:251], v121 offset:47104
	v_mfma_f32_16x16x32_bf16 v[76:79], v[252:255], v[216:219], v[76:79]
	v_pk_max_i16 v52, v52, 0
	v_pk_max_i16 v53, v53, 0
	v_mfma_f32_16x16x32_bf16 v[72:75], v[252:255], v[220:223], v[72:75]
	v_pk_max_i16 v54, v54, 0
	v_pk_max_i16 v55, v55, 0
	ds_read_b128 v[252:255], v121 offset:48128
	s_setprio 3
	s_waitcnt lgkmcnt(6)
	v_mfma_f32_16x16x32_bf16 v[64:67], v[224:227], v[0:3], v[152:155]
	v_mfma_f32_16x16x32_bf16 v[68:71], v[228:231], v[0:3], v[156:159]
	v_mfma_f32_16x16x32_bf16 v[60:63], v[228:231], v[4:7], v[156:159]
	v_mfma_f32_16x16x32_bf16 v[56:59], v[224:227], v[4:7], v[152:155]
	ds_read_b128 v[224:227], v121 offset:49152
	ds_read_b128 v[228:231], v121 offset:50176
	s_waitcnt lgkmcnt(6)
	ds_read_b128 v[160:163], v183 offset:128
	ds_read_b128 v[164:167], v183 offset:192
	v_mfma_f32_16x16x32_bf16 v[64:67], v[232:235], v[12:15], v[64:67]
	v_cvt_pk_bf16_f32 v112, v80, v81
	v_mfma_f32_16x16x32_bf16 v[68:71], v[236:239], v[12:15], v[68:71]
	s_mov_b32 m0, s35
	s_add_i32 s51, s50, 0x0
	v_cvt_pk_bf16_f32 v113, v82, v83
	v_mfma_f32_16x16x32_bf16 v[60:63], v[236:239], v[8:11], v[60:63]
	buffer_load_dwordx4 v125, s[36:39], s51 offen lds
	v_cvt_pk_bf16_f32 v114, v76, v77
	v_mfma_f32_16x16x32_bf16 v[56:59], v[232:235], v[8:11], v[56:59]
	v_cvt_pk_bf16_f32 v115, v78, v79
	ds_read_b128 v[232:235], v121 offset:51200
	ds_read_b128 v[236:239], v121 offset:52224
	s_waitcnt lgkmcnt(8)
	v_mfma_f32_16x16x32_bf16 v[64:67], v[240:243], v[16:19], v[64:67]
	v_cvt_pk_bf16_f32 v116, v84, v85
	v_mfma_f32_16x16x32_bf16 v[68:71], v[244:247], v[16:19], v[68:71]
	s_mov_b32 m0, s42
	s_add_i32 s51, s50, 0x2000
	v_cvt_pk_bf16_f32 v117, v86, v87
	v_mfma_f32_16x16x32_bf16 v[60:63], v[244:247], v[20:23], v[60:63]
	buffer_load_dwordx4 v125, s[36:39], s51 offen lds
	v_cvt_pk_bf16_f32 v118, v72, v73
	v_mfma_f32_16x16x32_bf16 v[56:59], v[240:243], v[20:23], v[56:59]
	v_cvt_pk_bf16_f32 v119, v74, v75
	ds_read_b128 v[240:243], v121 offset:53248
	ds_read_b128 v[244:247], v121 offset:54272
	s_waitcnt lgkmcnt(8)
	v_mfma_f32_16x16x32_bf16 v[64:67], v[248:251], v[24:27], v[64:67]
	v_pk_max_i16 v112, v112, 0
	v_mfma_f32_16x16x32_bf16 v[68:71], v[252:255], v[24:27], v[68:71]
	s_mov_b32 m0, s41
	s_add_i32 s51, s50, 0x4000
	v_pk_max_i16 v113, v113, 0
	v_mfma_f32_16x16x32_bf16 v[60:63], v[252:255], v[28:31], v[60:63]
	buffer_load_dwordx4 v125, s[36:39], s51 offen lds
	v_pk_max_i16 v114, v114, 0
	v_mfma_f32_16x16x32_bf16 v[56:59], v[248:251], v[28:31], v[56:59]
	v_pk_max_i16 v115, v115, 0
	ds_read_b128 v[248:251], v121 offset:55296
	ds_read_b128 v[252:255], v121 offset:56320
	s_setprio 2
	s_waitcnt lgkmcnt(8)
	v_mfma_f32_16x16x32_bf16 v[64:67], v[224:227], v[32:35], v[64:67]
	v_pk_max_i16 v116, v116, 0
	v_mfma_f32_16x16x32_bf16 v[68:71], v[228:231], v[32:35], v[68:71]
	s_mov_b32 m0, s40
	s_add_i32 s51, s50, 0x6000
	v_pk_max_i16 v117, v117, 0
	v_mfma_f32_16x16x32_bf16 v[60:63], v[228:231], v[36:39], v[60:63]
	buffer_load_dwordx4 v125, s[36:39], s51 offen lds
	v_pk_max_i16 v118, v118, 0
	v_mfma_f32_16x16x32_bf16 v[56:59], v[224:227], v[36:39], v[56:59]
	v_pk_max_i16 v119, v119, 0
	ds_read_b128 v[224:227], v121 offset:57344
	ds_read_b128 v[228:231], v121 offset:58368
	s_waitcnt lgkmcnt(6)
	v_mfma_f32_16x16x32_bf16 v[64:67], v[232:235], v[40:43], v[64:67]
	v_mfma_f32_16x16x32_bf16 v[68:71], v[236:239], v[40:43], v[68:71]
	v_mfma_f32_16x16x32_bf16 v[60:63], v[236:239], v[44:47], v[60:63]
	v_mfma_f32_16x16x32_bf16 v[56:59], v[232:235], v[44:47], v[56:59]
	ds_read_b128 v[232:235], v121 offset:59392
	ds_read_b128 v[236:239], v121 offset:60416
	s_waitcnt lgkmcnt(6)
	ds_read_b128 v[152:155], v183 offset:256
	ds_read_b128 v[156:159], v183 offset:320
	v_mfma_f32_16x16x32_bf16 v[64:67], v[240:243], v[48:51], v[64:67]
	v_mfma_f32_16x16x32_bf16 v[68:71], v[244:247], v[48:51], v[68:71]
	v_mfma_f32_16x16x32_bf16 v[60:63], v[244:247], v[52:55], v[60:63]
	v_mfma_f32_16x16x32_bf16 v[56:59], v[240:243], v[52:55], v[56:59]
	ds_read_b128 v[240:243], v121 offset:61440
	ds_read_b128 v[244:247], v121 offset:62464
	s_waitcnt lgkmcnt(8)
	v_mfma_f32_16x16x32_bf16 v[64:67], v[248:251], v[112:115], v[64:67]
	v_mfma_f32_16x16x32_bf16 v[68:71], v[252:255], v[112:115], v[68:71]
	v_mfma_f32_16x16x32_bf16 v[60:63], v[252:255], v[116:119], v[60:63]
	v_mfma_f32_16x16x32_bf16 v[56:59], v[248:251], v[116:119], v[56:59]
	ds_read_b128 v[248:251], v121 offset:63488
	ds_read_b128 v[252:255], v121 offset:64512
	s_setprio 1
	s_waitcnt lgkmcnt(8)
	v_mfma_f32_16x16x32_bf16 v[80:83], v[224:227], v[0:3], v[160:163]
	v_mfma_f32_16x16x32_bf16 v[76:79], v[228:231], v[0:3], v[164:167]
	v_mfma_f32_16x16x32_bf16 v[72:75], v[228:231], v[4:7], v[164:167]
	v_mfma_f32_16x16x32_bf16 v[84:87], v[224:227], v[4:7], v[160:163]
	ds_read_b128 v[224:227], v126 offset:57344
	ds_read_b128 v[228:231], v126 offset:58368
	s_waitcnt lgkmcnt(8)
	v_mfma_f32_16x16x32_bf16 v[80:83], v[232:235], v[12:15], v[80:83]
	v_cvt_pk_bf16_f32 v88, v64, v65
	v_mfma_f32_16x16x32_bf16 v[76:79], v[236:239], v[12:15], v[76:79]
	v_cvt_pk_bf16_f32 v89, v66, v67
	v_mfma_f32_16x16x32_bf16 v[72:75], v[236:239], v[8:11], v[72:75]
	v_cvt_pk_bf16_f32 v90, v68, v69
	v_mfma_f32_16x16x32_bf16 v[84:87], v[232:235], v[8:11], v[84:87]
	v_cvt_pk_bf16_f32 v91, v70, v71
	ds_read_b128 v[232:235], v126 offset:59392
	ds_read_b128 v[236:239], v126 offset:60416
	s_waitcnt lgkmcnt(6)
	v_mfma_f32_16x16x32_bf16 v[80:83], v[240:243], v[16:19], v[80:83]
	v_cvt_pk_bf16_f32 v92, v56, v57
	v_mfma_f32_16x16x32_bf16 v[76:79], v[244:247], v[16:19], v[76:79]
	v_cvt_pk_bf16_f32 v93, v58, v59
	v_mfma_f32_16x16x32_bf16 v[72:75], v[244:247], v[20:23], v[72:75]
	v_cvt_pk_bf16_f32 v94, v60, v61
	v_mfma_f32_16x16x32_bf16 v[84:87], v[240:243], v[20:23], v[84:87]
	v_cvt_pk_bf16_f32 v95, v62, v63
	ds_read_b128 v[240:243], v126 offset:61440
	ds_read_b128 v[244:247], v126 offset:62464
	s_waitcnt lgkmcnt(6)
	v_mfma_f32_16x16x32_bf16 v[80:83], v[248:251], v[24:27], v[80:83]
	v_pk_max_i16 v88, v88, 0
	v_mfma_f32_16x16x32_bf16 v[76:79], v[252:255], v[24:27], v[76:79]
	v_pk_max_i16 v89, v89, 0
	v_mfma_f32_16x16x32_bf16 v[72:75], v[252:255], v[28:31], v[72:75]
	v_pk_max_i16 v90, v90, 0
	v_mfma_f32_16x16x32_bf16 v[84:87], v[248:251], v[28:31], v[84:87]
	v_pk_max_i16 v91, v91, 0
	ds_read_b128 v[248:251], v126 offset:63488
	ds_read_b128 v[252:255], v126 offset:64512
	s_setprio 0
	s_waitcnt lgkmcnt(6)
	v_mfma_f32_16x16x32_bf16 v[80:83], v[224:227], v[32:35], v[80:83]
	v_pk_max_i16 v92, v92, 0
	v_mfma_f32_16x16x32_bf16 v[76:79], v[228:231], v[32:35], v[76:79]
	v_pk_max_i16 v93, v93, 0
	v_mfma_f32_16x16x32_bf16 v[72:75], v[228:231], v[36:39], v[72:75]
	v_pk_max_i16 v94, v94, 0
	v_mfma_f32_16x16x32_bf16 v[84:87], v[224:227], v[36:39], v[84:87]
	v_pk_max_i16 v95, v95, 0
	s_waitcnt lgkmcnt(4)
	v_mfma_f32_16x16x32_bf16 v[80:83], v[232:235], v[40:43], v[80:83]
	v_mfma_f32_16x16x32_bf16 v[76:79], v[236:239], v[40:43], v[76:79]
	v_mfma_f32_16x16x32_bf16 v[72:75], v[236:239], v[44:47], v[72:75]
	v_mfma_f32_16x16x32_bf16 v[84:87], v[232:235], v[44:47], v[84:87]
	s_branch .Lnerf_hid_a1

.Lnerf_hid_b_first:
	s_waitcnt vmcnt(0) lgkmcnt(0)
	s_barrier
	ds_read_b128 v[224:227], v121 offset:40960
	ds_read_b128 v[228:231], v121 offset:41984
	ds_read_b128 v[152:155], v183 offset:0
	ds_read_b128 v[156:159], v183 offset:64
	v_mfma_f32_16x16x32_bf16 v[80:83], v[240:243], v[208:211], 0
	ds_read_b128 v[232:235], v121 offset:43008
	v_cvt_pk_bf16_f32 v48, v64, v65
	v_cvt_pk_bf16_f32 v49, v66, v67
	v_mfma_f32_16x16x32_bf16 v[84:87], v[240:243], v[212:215], 0
	ds_read_b128 v[236:239], v121 offset:44032
	v_cvt_pk_bf16_f32 v52, v56, v57
	v_cvt_pk_bf16_f32 v53, v58, v59
	ds_read_b128 v[240:243], v121 offset:45056
	v_mfma_f32_16x16x32_bf16 v[76:79], v[244:247], v[208:211], 0
	v_cvt_pk_bf16_f32 v50, v68, v69
	v_cvt_pk_bf16_f32 v51, v70, v71
	v_mfma_f32_16x16x32_bf16 v[72:75], v[244:247], v[212:215], 0
	v_cvt_pk_bf16_f32 v54, v60, v61
	v_cvt_pk_bf16_f32 v55, v62, v63
	ds_read_b128 v[244:247], v121 offset:46080
	v_mfma_f32_16x16x32_bf16 v[80:83], v[248:251], v[216:219], v[80:83]
	v_pk_max_i16 v48, v48, 0
	v_pk_max_i16 v49, v49, 0
	v_mfma_f32_16x16x32_bf16 v[84:87], v[248:251], v[220:223], v[84:87]
	v_pk_max_i16 v50, v50, 0
	v_pk_max_i16 v51, v51, 0
	ds_read_b128 v[248:251], v121 offset:47104
	v_mfma_f32_16x16x32_bf16 v[76:79], v[252:255], v[216:219], v[76:79]
	v_pk_max_i16 v52, v52, 0
	v_pk_max_i16 v53, v53, 0
	v_mfma_f32_16x16x32_bf16 v[72:75], v[252:255], v[220:223], v[72:75]
	v_pk_max_i16 v54, v54, 0
	v_pk_max_i16 v55, v55, 0
	ds_read_b128 v[252:255], v121 offset:48128
	s_setprio 3
	s_waitcnt lgkmcnt(6)
	v_mfma_f32_16x16x32_bf16 v[64:67], v[224:227], v[0:3], v[152:155]
	v_mfma_f32_16x16x32_bf16 v[68:71], v[228:231], v[0:3], v[156:159]
	v_mfma_f32_16x16x32_bf16 v[60:63], v[228:231], v[4:7], v[156:159]
	v_mfma_f32_16x16x32_bf16 v[56:59], v[224:227], v[4:7], v[152:155]
	ds_read_b128 v[224:227], v121 offset:49152
	ds_read_b128 v[228:231], v121 offset:50176
	s_waitcnt lgkmcnt(6)
	ds_read_b128 v[160:163], v183 offset:128
	ds_read_b128 v[164:167], v183 offset:192
	v_mfma_f32_16x16x32_bf16 v[64:67], v[232:235], v[12:15], v[64:67]
	v_cvt_pk_bf16_f32 v112, v80, v81
	v_mfma_f32_16x16x32_bf16 v[68:71], v[236:239], v[12:15], v[68:71]
	v_cvt_pk_bf16_f32 v113, v82, v83
	v_mfma_f32_16x16x32_bf16 v[60:63], v[236:239], v[8:11], v[60:63]
	v_cvt_pk_bf16_f32 v114, v76, v77
	v_mfma_f32_16x16x32_bf16 v[56:59], v[232:235], v[8:11], v[56:59]
	v_cvt_pk_bf16_f32 v115, v78, v79
	ds_read_b128 v[232:235], v121 offset:51200
	ds_read_b128 v[236:239], v121 offset:52224
	s_waitcnt lgkmcnt(8)
	v_mfma_f32_16x16x32_bf16 v[64:67], v[240:243], v[16:19], v[64:67]
	v_cvt_pk_bf16_f32 v116, v84, v85
	v_mfma_f32_16x16x32_bf16 v[68:71], v[244:247], v[16:19], v[68:71]
	v_cvt_pk_bf16_f32 v117, v86, v87
	v_mfma_f32_16x16x32_bf16 v[60:63], v[244:247], v[20:23], v[60:63]
	v_cvt_pk_bf16_f32 v118, v72, v73
	v_mfma_f32_16x16x32_bf16 v[56:59], v[240:243], v[20:23], v[56:59]
	v_cvt_pk_bf16_f32 v119, v74, v75
	ds_read_b128 v[240:243], v121 offset:53248
	ds_read_b128 v[244:247], v121 offset:54272
	s_waitcnt lgkmcnt(8)
	v_mfma_f32_16x16x32_bf16 v[64:67], v[248:251], v[24:27], v[64:67]
	v_pk_max_i16 v112, v112, 0
	v_mfma_f32_16x16x32_bf16 v[68:71], v[252:255], v[24:27], v[68:71]
	v_pk_max_i16 v113, v113, 0
	v_mfma_f32_16x16x32_bf16 v[60:63], v[252:255], v[28:31], v[60:63]
	v_pk_max_i16 v114, v114, 0
	v_mfma_f32_16x16x32_bf16 v[56:59], v[248:251], v[28:31], v[56:59]
	v_pk_max_i16 v115, v115, 0
	ds_read_b128 v[248:251], v121 offset:55296
	ds_read_b128 v[252:255], v121 offset:56320
	s_setprio 2
	s_waitcnt lgkmcnt(8)
	v_mfma_f32_16x16x32_bf16 v[64:67], v[224:227], v[32:35], v[64:67]
	v_pk_max_i16 v116, v116, 0
	v_mfma_f32_16x16x32_bf16 v[68:71], v[228:231], v[32:35], v[68:71]
	v_pk_max_i16 v117, v117, 0
	v_mfma_f32_16x16x32_bf16 v[60:63], v[228:231], v[36:39], v[60:63]
	v_pk_max_i16 v118, v118, 0
	v_mfma_f32_16x16x32_bf16 v[56:59], v[224:227], v[36:39], v[56:59]
	v_pk_max_i16 v119, v119, 0
	ds_read_b128 v[224:227], v121 offset:57344
	ds_read_b128 v[228:231], v121 offset:58368
	s_waitcnt lgkmcnt(6)
	v_mfma_f32_16x16x32_bf16 v[64:67], v[232:235], v[40:43], v[64:67]
	v_mfma_f32_16x16x32_bf16 v[68:71], v[236:239], v[40:43], v[68:71]
	s_mov_b32 m0, s35
	s_add_i32 s51, s50, 0x0
	v_mfma_f32_16x16x32_bf16 v[60:63], v[236:239], v[44:47], v[60:63]
	buffer_load_dwordx4 v125, s[36:39], s51 offen lds
	v_mfma_f32_16x16x32_bf16 v[56:59], v[232:235], v[44:47], v[56:59]
	ds_read_b128 v[232:235], v121 offset:59392
	ds_read_b128 v[236:239], v121 offset:60416
	s_waitcnt lgkmcnt(6)
	ds_read_b128 v[152:155], v183 offset:256
	ds_read_b128 v[156:159], v183 offset:320
	v_mfma_f32_16x16x32_bf16 v[64:67], v[240:243], v[48:51], v[64:67]
	v_mfma_f32_16x16x32_bf16 v[68:71], v[244:247], v[48:51], v[68:71]
	s_mov_b32 m0, s42
	s_add_i32 s51, s50, 0x2000
	v_mfma_f32_16x16x32_bf16 v[60:63], v[244:247], v[52:55], v[60:63]
	buffer_load_dwordx4 v125, s[36:39], s51 offen lds
	v_mfma_f32_16x16x32_bf16 v[56:59], v[240:243], v[52:55], v[56:59]
	ds_read_b128 v[240:243], v121 offset:61440
	ds_read_b128 v[244:247], v121 offset:62464
	s_waitcnt lgkmcnt(8)
	v_mfma_f32_16x16x32_bf16 v[64:67], v[248:251], v[112:115], v[64:67]
	v_mfma_f32_16x16x32_bf16 v[68:71], v[252:255], v[112:115], v[68:71]
	s_mov_b32 m0, s41
	s_add_i32 s51, s50, 0x4000
	v_mfma_f32_16x16x32_bf16 v[60:63], v[252:255], v[116:119], v[60:63]
	buffer_load_dwordx4 v125, s[36:39], s51 offen lds
	v_mfma_f32_16x16x32_bf16 v[56:59], v[248:251], v[116:119], v[56:59]
	ds_read_b128 v[248:251], v121 offset:63488
	ds_read_b128 v[252:255], v121 offset:64512
	s_setprio 1
	s_waitcnt lgkmcnt(8)
	v_mfma_f32_16x16x32_bf16 v[80:83], v[224:227], v[0:3], v[160:163]
	v_mfma_f32_16x16x32_bf16 v[76:79], v[228:231], v[0:3], v[164:167]
	s_mov_b32 m0, s40
	s_add_i32 s51, s50, 0x6000
	v_mfma_f32_16x16x32_bf16 v[72:75], v[228:231], v[4:7], v[164:167]
	buffer_load_dwordx4 v125, s[36:39], s51 offen lds
	v_mfma_f32_16x16x32_bf16 v[84:87], v[224:227], v[4:7], v[160:163]
	ds_read_b128 v[224:227], v126 offset:57344
	ds_read_b128 v[228:231], v126 offset:58368
	s_waitcnt lgkmcnt(8)
	v_mfma_f32_16x16x32_bf16 v[80:83], v[232:235], v[12:15], v[80:83]
	v_cvt_pk_bf16_f32 v88, v64, v65
	v_mfma_f32_16x16x32_bf16 v[76:79], v[236:239], v[12:15], v[76:79]
	v_cvt_pk_bf16_f32 v89, v66, v67
	v_mfma_f32_16x16x32_bf16 v[72:75], v[236:239], v[8:11], v[72:75]
	v_cvt_pk_bf16_f32 v90, v68, v69
	v_mfma_f32_16x16x32_bf16 v[84:87], v[232:235], v[8:11], v[84:87]
	v_cvt_pk_bf16_f32 v91, v70, v71
	ds_read_b128 v[232:235], v126 offset:59392
	ds_read_b128 v[236:239], v126 offset:60416
	s_waitcnt lgkmcnt(6)
	v_mfma_f32_16x16x32_bf16 v[80:83], v[240:243], v[16:19], v[80:83]
	v_cvt_pk_bf16_f32 v92, v56, v57
	v_mfma_f32_16x16x32_bf16 v[76:79], v[244:247], v[16:19], v[76:79]
	v_cvt_pk_bf16_f32 v93, v58, v59
	v_mfma_f32_16x16x32_bf16 v[72:75], v[244:247], v[20:23], v[72:75]
	v_cvt_pk_bf16_f32 v94, v60, v61
	v_mfma_f32_16x16x32_bf16 v[84:87], v[240:243], v[20:23], v[84:87]
	v_cvt_pk_bf16_f32 v95, v62, v63
	ds_read_b128 v[240:243], v126 offset:61440
	ds_read_b128 v[244:247], v126 offset:62464
	s_waitcnt lgkmcnt(6)
	v_mfma_f32_16x16x32_bf16 v[80:83], v[248:251], v[24:27], v[80:83]
	v_pk_max_i16 v88, v88, 0
	v_mfma_f32_16x16x32_bf16 v[76:79], v[252:255], v[24:27], v[76:79]
	v_pk_max_i16 v89, v89, 0
	v_mfma_f32_16x16x32_bf16 v[72:75], v[252:255], v[28:31], v[72:75]
	v_pk_max_i16 v90, v90, 0
	v_mfma_f32_16x16x32_bf16 v[84:87], v[248:251], v[28:31], v[84:87]
	v_pk_max_i16 v91, v91, 0
	ds_read_b128 v[248:251], v126 offset:63488
	ds_read_b128 v[252:255], v126 offset:64512
	s_setprio 0
	s_waitcnt lgkmcnt(6)
	v_mfma_f32_16x16x32_bf16 v[80:83], v[224:227], v[32:35], v[80:83]
	v_pk_max_i16 v92, v92, 0
	v_mfma_f32_16x16x32_bf16 v[76:79], v[228:231], v[32:35], v[76:79]
	v_pk_max_i16 v93, v93, 0
	v_mfma_f32_16x16x32_bf16 v[72:75], v[228:231], v[36:39], v[72:75]
	v_pk_max_i16 v94, v94, 0
	v_mfma_f32_16x16x32_bf16 v[84:87], v[224:227], v[36:39], v[84:87]
	v_pk_max_i16 v95, v95, 0
	s_waitcnt lgkmcnt(4)
	v_mfma_f32_16x16x32_bf16 v[80:83], v[232:235], v[40:43], v[80:83]
	v_mfma_f32_16x16x32_bf16 v[76:79], v[236:239], v[40:43], v[76:79]
	v_mfma_f32_16x16x32_bf16 v[72:75], v[236:239], v[44:47], v[72:75]
	v_mfma_f32_16x16x32_bf16 v[84:87], v[232:235], v[44:47], v[84:87]
	s_branch .Lnerf_hid_b1

.Lnerf_head:
	s_waitcnt lgkmcnt(0)
	ds_read_b128 v[224:227], v149 offset:0
	ds_read_b128 v[228:231], v149 offset:1024
	ds_read_b128 v[4:7], v183 offset:1024
	ds_read_b128 v[0:3], v183 offset:1024
	v_mfma_f32_16x16x32_bf16 v[80:83], v[240:243], v[48:51], v[80:83]
	ds_read_b128 v[232:235], v149 offset:2048
	v_mfma_f32_16x16x32_bf16 v[76:79], v[244:247], v[48:51], v[76:79]
	ds_read_b128 v[236:239], v149 offset:3072
	v_mfma_f32_16x16x32_bf16 v[72:75], v[244:247], v[52:55], v[72:75]
	v_mfma_f32_16x16x32_bf16 v[84:87], v[240:243], v[52:55], v[84:87]
	ds_read_b128 v[240:243], v149 offset:4096
	ds_read_b128 v[244:247], v149 offset:5120
	v_mfma_f32_16x16x32_bf16 v[80:83], v[248:251], v[112:115], v[80:83]
	v_mfma_f32_16x16x32_bf16 v[76:79], v[252:255], v[112:115], v[76:79]
	v_mfma_f32_16x16x32_bf16 v[72:75], v[252:255], v[116:119], v[72:75]
	v_mfma_f32_16x16x32_bf16 v[84:87], v[248:251], v[116:119], v[84:87]
	ds_read_b128 v[248:251], v149 offset:6144
	ds_read_b128 v[252:255], v149 offset:7168
	s_waitcnt lgkmcnt(7)
	v_mfma_f32_16x16x32_bf16 v[4:7], v[224:227], v[88:91], v[4:7]
	s_waitcnt lgkmcnt(6)
	v_mfma_f32_16x16x32_bf16 v[0:3], v[224:227], v[92:95], v[0:3]
	v_cvt_pk_bf16_f32 v216, v80, v81
	v_cvt_pk_bf16_f32 v217, v82, v83
	v_mfma_f32_16x16x32_bf16 v[4:7], v[228:231], v[96:99], v[4:7]
	v_cvt_pk_bf16_f32 v218, v76, v77
	v_cvt_pk_bf16_f32 v219, v78, v79
	v_mfma_f32_16x16x32_bf16 v[0:3], v[228:231], v[100:103], v[0:3]
	v_cvt_pk_bf16_f32 v220, v84, v85
	v_cvt_pk_bf16_f32 v221, v86, v87
	s_waitcnt lgkmcnt(5)
	v_mfma_f32_16x16x32_bf16 v[4:7], v[232:235], v[104:107], v[4:7]
	v_cvt_pk_bf16_f32 v222, v72, v73
	v_cvt_pk_bf16_f32 v223, v74, v75
	v_mfma_f32_16x16x32_bf16 v[0:3], v[232:235], v[108:111], v[0:3]
	v_pk_max_i16 v216, v216, 0
	v_pk_max_i16 v217, v217, 0
	s_waitcnt lgkmcnt(4)
	v_mfma_f32_16x16x32_bf16 v[4:7], v[236:239], v[184:187], v[4:7]
	v_pk_max_i16 v218, v218, 0
	v_pk_max_i16 v219, v219, 0
	v_mfma_f32_16x16x32_bf16 v[0:3], v[236:239], v[188:191], v[0:3]
	v_pk_max_i16 v220, v220, 0
	v_pk_max_i16 v221, v221, 0
	s_waitcnt lgkmcnt(3)
	v_mfma_f32_16x16x32_bf16 v[4:7], v[240:243], v[192:195], v[4:7]
	v_pk_max_i16 v222, v222, 0
	v_pk_max_i16 v223, v223, 0
	v_mfma_f32_16x16x32_bf16 v[0:3], v[240:243], v[196:199], v[0:3]
	s_waitcnt lgkmcnt(2)
	v_mfma_f32_16x16x32_bf16 v[4:7], v[244:247], v[200:203], v[4:7]
	v_mfma_f32_16x16x32_bf16 v[0:3], v[244:247], v[204:207], v[0:3]
	s_waitcnt lgkmcnt(1)
	v_mfma_f32_16x16x32_bf16 v[4:7], v[248:251], v[208:211], v[4:7]
	v_mfma_f32_16x16x32_bf16 v[0:3], v[248:251], v[212:215], v[0:3]
	s_nop 1
	s_waitcnt lgkmcnt(0)
	v_mfma_f32_16x16x32_bf16 v[4:7], v[252:255], v[216:219], v[4:7]
	v_mfma_f32_16x16x32_bf16 v[0:3], v[252:255], v[220:223], v[0:3]
	s_nop 7
	s_nop 1
	s_setprio 0
	s_and_saveexec_b64 s[20:21], s[2:3]
	s_cbranch_execz .LBB1_20
	s_nop 4
	v_mul_f32_e32 v6, 0xbfb8aa3b, v6
	v_mul_f32_e32 v7, 0xbfb8aa3b, v7
	v_mul_f32_e32 v4, 0xbfb8aa3b, v4
	v_mul_f32_e32 v5, 0xbfb8aa3b, v5
	v_exp_f32_e32 v6, v6
	v_exp_f32_e32 v7, v7
	v_exp_f32_e32 v4, v4
	v_exp_f32_e32 v5, v5
	s_lshl_b32 s24, s45, 6
	s_add_i32 s47, s43, s24
	s_nop 0
	v_add_f32_e32 v6, 1.0, v6
	v_add_f32_e32 v7, 1.0, v7
	v_add_f32_e32 v4, 1.0, v4
	v_add_f32_e32 v5, 1.0, v5
	v_rcp_f32_e32 v6, v6
	v_rcp_f32_e32 v7, v7
	v_rcp_f32_e32 v4, v4
	v_rcp_f32_e32 v5, v5
	s_mov_b64 s[24:25], -1
	s_nop 0
	s_and_b64 vcc, exec, s[16:17]
	s_cbranch_vccz .LBB1_14
	v_or_b32_e32 v8, s47, v130
	v_lshl_add_u32 v8, v8, 4, v182
	ds_write_b128 v8, v[4:7]
	s_mov_b64 s[24:25], 0

	.amdhsa_kernel _Z9nerf_mainPKfS0_S0_PKiS2_PKcS0_Pf
		.amdhsa_group_segment_fixed_size 147456
		.amdhsa_private_segment_fixed_size 0
		.amdhsa_kernarg_size 64
		.amdhsa_user_sgpr_count 2
		.amdhsa_user_sgpr_dispatch_ptr 0
		.amdhsa_user_sgpr_queue_ptr 0
		.amdhsa_user_sgpr_kernarg_segment_ptr 1
		.amdhsa_user_sgpr_dispatch_id 0
		.amdhsa_user_sgpr_kernarg_preload_length 0
		.amdhsa_user_sgpr_kernarg_preload_offset 0
		.amdhsa_user_sgpr_private_segment_size 0
		.amdhsa_uses_dynamic_stack 0
		.amdhsa_enable_private_segment 0
		.amdhsa_system_sgpr_workgroup_id_x 1
		.amdhsa_system_sgpr_workgroup_id_y 0
		.amdhsa_system_sgpr_workgroup_id_z 0
		.amdhsa_system_sgpr_workgroup_info 0
		.amdhsa_system_vgpr_workitem_id 0
		.amdhsa_next_free_vgpr 256
		.amdhsa_next_free_sgpr 96
		.amdhsa_accum_offset 256
		.amdhsa_reserve_vcc 1
		.amdhsa_float_round_mode_32 0
		.amdhsa_float_round_mode_16_64 0
		.amdhsa_float_denorm_mode_32 3
		.amdhsa_float_denorm_mode_16_64 3
		.amdhsa_dx10_clamp 1
		.amdhsa_ieee_mode 1
		.amdhsa_fp16_overflow 0
		.amdhsa_tg_split 0
		.amdhsa_exception_fp_ieee_invalid_op 0
		.amdhsa_exception_fp_denorm_src 0
		.amdhsa_exception_fp_ieee_div_zero 0
		.amdhsa_exception_fp_ieee_overflow 0
		.amdhsa_exception_fp_ieee_underflow 0
		.amdhsa_exception_fp_ieee_inexact 0
		.amdhsa_exception_int_div_zero 0
	.end_amdhsa_kernel

amdhsa.kernels:
  - .agpr_count:     0
    .args:
      - .actual_access:  read_only
        .address_space:  global
        .offset:         0
        .size:           8
        .value_kind:     global_buffer
      - .actual_access:  read_only
        .address_space:  global
        .offset:         8
        .size:           8
        .value_kind:     global_buffer
      - .actual_access:  read_only
        .address_space:  global
        .offset:         16
        .size:           8
        .value_kind:     global_buffer
      - .actual_access:  read_only
        .address_space:  global
        .offset:         24
        .size:           8
        .value_kind:     global_buffer
      - .actual_access:  read_only
        .address_space:  global
        .offset:         32
        .size:           8
        .value_kind:     global_buffer
      - .actual_access:  read_only
        .address_space:  global
        .offset:         40
        .size:           8
        .value_kind:     global_buffer
      - .actual_access:  read_only
        .address_space:  global
        .offset:         48
        .size:           8
        .value_kind:     global_buffer
      - .actual_access:  read_only
        .address_space:  global
        .offset:         56
        .size:           8
        .value_kind:     global_buffer
      - .actual_access:  read_only
        .address_space:  global
        .offset:         64
        .size:           8
        .value_kind:     global_buffer
      - .actual_access:  read_only
        .address_space:  global
        .offset:         72
        .size:           8
        .value_kind:     global_buffer
      - .actual_access:  read_only
        .address_space:  global
        .offset:         80
        .size:           8
        .value_kind:     global_buffer
      - .actual_access:  write_only
        .address_space:  global
        .offset:         88
        .size:           8
        .value_kind:     global_buffer
      - .actual_access:  write_only
        .address_space:  global
        .offset:         96
        .size:           8
        .value_kind:     global_buffer
    .group_segment_fixed_size: 0
    .kernarg_segment_align: 8
    .kernarg_segment_size: 104
    .language:       OpenCL C
    .language_version:
      - 2
      - 0
    .max_flat_workgroup_size: 256
    .name:           _Z9nerf_prepPKfS0_S0_S0_S0_S0_S0_S0_S0_S0_S0_PtPf
    .private_segment_fixed_size: 0
    .sgpr_count:     26
    .sgpr_spill_count: 0
    .symbol:         _Z9nerf_prepPKfS0_S0_S0_S0_S0_S0_S0_S0_S0_S0_PtPf.kd
    .uniform_work_group_size: 1
    .uses_dynamic_stack: false
    .vgpr_count:     54
    .vgpr_spill_count: 0
    .wavefront_size: 64
  - .agpr_count:     0
    .args:
      - .actual_access:  read_only
        .address_space:  global
        .offset:         0
        .size:           8
        .value_kind:     global_buffer
      - .actual_access:  read_only
        .address_space:  global
        .offset:         8
        .size:           8
        .value_kind:     global_buffer
      - .actual_access:  read_only
        .address_space:  global
        .offset:         16
        .size:           8
        .value_kind:     global_buffer
      - .actual_access:  read_only
        .address_space:  global
        .offset:         24
        .size:           8
        .value_kind:     global_buffer
      - .actual_access:  read_only
        .address_space:  global
        .offset:         32
        .size:           8
        .value_kind:     global_buffer
      - .actual_access:  read_only
        .address_space:  global
        .offset:         40
        .size:           8
        .value_kind:     global_buffer
      - .actual_access:  read_only
        .address_space:  global
        .offset:         48
        .size:           8
        .value_kind:     global_buffer
      - .actual_access:  write_only
        .address_space:  global
        .offset:         56
        .size:           8
        .value_kind:     global_buffer
    .group_segment_fixed_size: 147456
    .kernarg_segment_align: 8
    .kernarg_segment_size: 64
    .language:       OpenCL C
    .language_version:
      - 2
      - 0
    .max_flat_workgroup_size: 512
    .name:           _Z9nerf_mainPKfS0_S0_PKiS2_PKcS0_Pf
    .private_segment_fixed_size: 0
    .sgpr_count:     55
    .sgpr_spill_count: 0
    .symbol:         _Z9nerf_mainPKfS0_S0_PKiS2_PKcS0_Pf.kd
    .uniform_work_group_size: 1
    .uses_dynamic_stack: false
    .vgpr_count:     256
    .vgpr_spill_count: 0
    .wavefront_size: 64
